# t15
# baseline (speedup 1.0000x reference)
.LBB0_7:
	s_or_b64 exec, exec, s[0:1]
	s_waitcnt lgkmcnt(0)
	s_barrier
	ds_read_b128 v[0:3], v30
	s_add_u32 s0, s6, s4
	s_addc_u32 s1, s7, s5
	v_add_u32_e32 v14, v15, v14
	ds_read_b128 v[4:7], v14 offset:16384
	s_waitcnt lgkmcnt(1)
	global_store_dwordx4 v30, v[0:3], s[0:1] sc1 nt
	ds_read_b128 v[0:3], v14 offset:4096
	v_lshl_add_u64 v[16:17], s[0:1], 0, v[30:31]
	v_add_co_u32_e32 v12, vcc, 0x1000, v16
	ds_read_b128 v[8:11], v49
	s_nop 0
	v_addc_co_u32_e32 v13, vcc, 0, v17, vcc
	s_waitcnt lgkmcnt(1)
	global_store_dwordx4 v[12:13], v[0:3], off sc1 nt
	ds_read_b128 v[0:3], v14 offset:8192
	ds_read_b128 v[12:15], v14 offset:12288
	v_add_co_u32_e32 v18, vcc, 0x2000, v16
	s_nop 1
	v_addc_co_u32_e32 v19, vcc, 0, v17, vcc
	s_waitcnt lgkmcnt(1)
	global_store_dwordx4 v[18:19], v[0:3], off sc1 nt
	s_nop 1
	v_add_co_u32_e32 v0, vcc, 0x3000, v16
	s_nop 1
	v_addc_co_u32_e32 v1, vcc, 0, v17, vcc
	s_waitcnt lgkmcnt(0)
	global_store_dwordx4 v[0:1], v[12:15], off sc1 nt
	v_lshlrev_b32_e32 v0, 4, v48
	global_store_dwordx4 v0, v[4:7], s[0:1] sc1 nt
	global_store_dwordx4 v49, v[8:11], s[0:1] sc1 nt
	s_endpgm
